# exec-predication: indexer level-2 histogram pass rewritten as straight-line predicated code (compare, address, masked ds_add per key; 4 scalar group guards) replacing 136 exec branches in two interlea
# speedup vs baseline: 1.0155x; 1.0021x over previous
.LBB0_443:
	s_add_i32 s29, s37, 32
	s_cmp_gt_i32 s29, s81
	s_cselect_b64 s[18:19], -1, 0
	s_cbranch_scc1 .Lpb_nonext
	s_add_i32 s0, s37, 40
	s_cmp_gt_i32 s0, s81
	s_cselect_b32 s0, s29, s0
	v_lshl_add_u32 v8, s0, 11, v5
	s_add_i32 s0, s37, 48
	s_cmp_gt_i32 s0, s81
	s_cselect_b32 s0, s29, s0
	global_load_dwordx4 v[84:87], v7, s[12:13] offset:16
	global_load_dwordx4 v[88:91], v7, s[12:13]
	global_load_dwordx4 v[92:95], v8, s[12:13] offset:16
	global_load_dwordx4 v[96:99], v8, s[12:13]
	v_lshl_add_u32 v8, s0, 11, v5
	s_add_i32 s0, s37, 56
	s_cmp_gt_i32 s0, s81
	s_cselect_b32 s0, s29, s0
	global_load_dwordx4 v[108:111], v8, s[12:13] offset:16
	global_load_dwordx4 v[112:115], v8, s[12:13]
	v_lshl_add_u32 v8, s0, 11, v5
	global_load_dwordx4 v[124:127], v8, s[12:13] offset:16
	global_load_dwordx4 v[128:131], v8, s[12:13]
	s_waitcnt vmcnt(8) lgkmcnt(0)
	s_branch .Lpb_go
.Lpb_nonext:
	s_waitcnt vmcnt(0) lgkmcnt(0)
.Lpb_go:
	v_cmp_eq_u32_sdwa s[38:39], v208, v4 src0_sel:BYTE_1 src1_sel:DWORD
	v_and_b32_e32 v8, 0xff, v208
	v_lshl_add_u32 v8, v8, 2, v6
	s_and_saveexec_b64 s[0:1], s[38:39]
	ds_add_u32 v8, v224
	s_mov_b64 exec, s[0:1]
	v_cmp_eq_u32_sdwa s[38:39], v208, v4 src0_sel:BYTE_3 src1_sel:DWORD
	v_bfe_u32 v8, v208, 16, 8
	v_lshl_add_u32 v8, v8, 2, v6
	s_and_saveexec_b64 s[0:1], s[38:39]
	ds_add_u32 v8, v224
	s_mov_b64 exec, s[0:1]
	v_cmp_eq_u32_sdwa s[38:39], v209, v4 src0_sel:BYTE_1 src1_sel:DWORD
	v_and_b32_e32 v8, 0xff, v209
	v_lshl_add_u32 v8, v8, 2, v6
	s_and_saveexec_b64 s[0:1], s[38:39]
	ds_add_u32 v8, v224
	s_mov_b64 exec, s[0:1]
	v_cmp_eq_u32_sdwa s[38:39], v209, v4 src0_sel:BYTE_3 src1_sel:DWORD
	v_bfe_u32 v8, v209, 16, 8
	v_lshl_add_u32 v8, v8, 2, v6
	s_and_saveexec_b64 s[0:1], s[38:39]
	ds_add_u32 v8, v224
	s_mov_b64 exec, s[0:1]
	v_cmp_eq_u32_sdwa s[38:39], v210, v4 src0_sel:BYTE_1 src1_sel:DWORD
	v_and_b32_e32 v8, 0xff, v210
	v_lshl_add_u32 v8, v8, 2, v6
	s_and_saveexec_b64 s[0:1], s[38:39]
	ds_add_u32 v8, v224
	s_mov_b64 exec, s[0:1]
	v_cmp_eq_u32_sdwa s[38:39], v210, v4 src0_sel:BYTE_3 src1_sel:DWORD
	v_bfe_u32 v8, v210, 16, 8
	v_lshl_add_u32 v8, v8, 2, v6
	s_and_saveexec_b64 s[0:1], s[38:39]
	ds_add_u32 v8, v224
	s_mov_b64 exec, s[0:1]
	v_cmp_eq_u32_sdwa s[38:39], v211, v4 src0_sel:BYTE_1 src1_sel:DWORD
	v_and_b32_e32 v8, 0xff, v211
	v_lshl_add_u32 v8, v8, 2, v6
	s_and_saveexec_b64 s[0:1], s[38:39]
	ds_add_u32 v8, v224
	s_mov_b64 exec, s[0:1]
	v_cmp_eq_u32_sdwa s[38:39], v211, v4 src0_sel:BYTE_3 src1_sel:DWORD
	v_bfe_u32 v8, v211, 16, 8
	v_lshl_add_u32 v8, v8, 2, v6
	s_and_saveexec_b64 s[0:1], s[38:39]
	ds_add_u32 v8, v224
	s_mov_b64 exec, s[0:1]
	v_cmp_eq_u32_sdwa s[38:39], v204, v4 src0_sel:BYTE_1 src1_sel:DWORD
	v_and_b32_e32 v8, 0xff, v204
	v_lshl_add_u32 v8, v8, 2, v6
	s_and_saveexec_b64 s[0:1], s[38:39]
	ds_add_u32 v8, v224
	s_mov_b64 exec, s[0:1]
	v_cmp_eq_u32_sdwa s[38:39], v204, v4 src0_sel:BYTE_3 src1_sel:DWORD
	v_bfe_u32 v8, v204, 16, 8
	v_lshl_add_u32 v8, v8, 2, v6
	s_and_saveexec_b64 s[0:1], s[38:39]
	ds_add_u32 v8, v224
	s_mov_b64 exec, s[0:1]
	v_cmp_eq_u32_sdwa s[38:39], v205, v4 src0_sel:BYTE_1 src1_sel:DWORD
	v_and_b32_e32 v8, 0xff, v205
	v_lshl_add_u32 v8, v8, 2, v6
	s_and_saveexec_b64 s[0:1], s[38:39]
	ds_add_u32 v8, v224
	s_mov_b64 exec, s[0:1]
	v_cmp_eq_u32_sdwa s[38:39], v205, v4 src0_sel:BYTE_3 src1_sel:DWORD
	v_bfe_u32 v8, v205, 16, 8
	v_lshl_add_u32 v8, v8, 2, v6
	s_and_saveexec_b64 s[0:1], s[38:39]
	ds_add_u32 v8, v224
	s_mov_b64 exec, s[0:1]
	v_cmp_eq_u32_sdwa s[38:39], v206, v4 src0_sel:BYTE_1 src1_sel:DWORD
	v_and_b32_e32 v8, 0xff, v206
	v_lshl_add_u32 v8, v8, 2, v6
	s_and_saveexec_b64 s[0:1], s[38:39]
	ds_add_u32 v8, v224
	s_mov_b64 exec, s[0:1]
	v_cmp_eq_u32_sdwa s[38:39], v206, v4 src0_sel:BYTE_3 src1_sel:DWORD
	v_bfe_u32 v8, v206, 16, 8
	v_lshl_add_u32 v8, v8, 2, v6
	s_and_saveexec_b64 s[0:1], s[38:39]
	ds_add_u32 v8, v224
	s_mov_b64 exec, s[0:1]
	v_cmp_eq_u32_sdwa s[38:39], v207, v4 src0_sel:BYTE_1 src1_sel:DWORD
	v_and_b32_e32 v8, 0xff, v207
	v_lshl_add_u32 v8, v8, 2, v6
	s_and_saveexec_b64 s[0:1], s[38:39]
	ds_add_u32 v8, v224
	s_mov_b64 exec, s[0:1]
	v_cmp_eq_u32_sdwa s[38:39], v207, v4 src0_sel:BYTE_3 src1_sel:DWORD
	v_bfe_u32 v8, v207, 16, 8
	v_lshl_add_u32 v8, v8, 2, v6
	s_and_saveexec_b64 s[0:1], s[38:39]
	ds_add_u32 v8, v224
	s_mov_b64 exec, s[0:1]
	s_cmp_gt_i32 s37, s24
	s_cbranch_scc1 .Lpb_done
	v_cmp_eq_u32_sdwa s[38:39], v200, v4 src0_sel:BYTE_1 src1_sel:DWORD
	v_and_b32_e32 v8, 0xff, v200
	v_lshl_add_u32 v8, v8, 2, v6
	s_and_saveexec_b64 s[0:1], s[38:39]
	ds_add_u32 v8, v224
	s_mov_b64 exec, s[0:1]
	v_cmp_eq_u32_sdwa s[38:39], v200, v4 src0_sel:BYTE_3 src1_sel:DWORD
	v_bfe_u32 v8, v200, 16, 8
	v_lshl_add_u32 v8, v8, 2, v6
	s_and_saveexec_b64 s[0:1], s[38:39]
	ds_add_u32 v8, v224
	s_mov_b64 exec, s[0:1]
	v_cmp_eq_u32_sdwa s[38:39], v201, v4 src0_sel:BYTE_1 src1_sel:DWORD
	v_and_b32_e32 v8, 0xff, v201
	v_lshl_add_u32 v8, v8, 2, v6
	s_and_saveexec_b64 s[0:1], s[38:39]
	ds_add_u32 v8, v224
	s_mov_b64 exec, s[0:1]
	v_cmp_eq_u32_sdwa s[38:39], v201, v4 src0_sel:BYTE_3 src1_sel:DWORD
	v_bfe_u32 v8, v201, 16, 8
	v_lshl_add_u32 v8, v8, 2, v6
	s_and_saveexec_b64 s[0:1], s[38:39]
	ds_add_u32 v8, v224
	s_mov_b64 exec, s[0:1]
	v_cmp_eq_u32_sdwa s[38:39], v202, v4 src0_sel:BYTE_1 src1_sel:DWORD
	v_and_b32_e32 v8, 0xff, v202
	v_lshl_add_u32 v8, v8, 2, v6
	s_and_saveexec_b64 s[0:1], s[38:39]
	ds_add_u32 v8, v224
	s_mov_b64 exec, s[0:1]
	v_cmp_eq_u32_sdwa s[38:39], v202, v4 src0_sel:BYTE_3 src1_sel:DWORD
	v_bfe_u32 v8, v202, 16, 8
	v_lshl_add_u32 v8, v8, 2, v6
	s_and_saveexec_b64 s[0:1], s[38:39]
	ds_add_u32 v8, v224
	s_mov_b64 exec, s[0:1]
	v_cmp_eq_u32_sdwa s[38:39], v203, v4 src0_sel:BYTE_1 src1_sel:DWORD
	v_and_b32_e32 v8, 0xff, v203
	v_lshl_add_u32 v8, v8, 2, v6
	s_and_saveexec_b64 s[0:1], s[38:39]
	ds_add_u32 v8, v224
	s_mov_b64 exec, s[0:1]
	v_cmp_eq_u32_sdwa s[38:39], v203, v4 src0_sel:BYTE_3 src1_sel:DWORD
	v_bfe_u32 v8, v203, 16, 8
	v_lshl_add_u32 v8, v8, 2, v6
	s_and_saveexec_b64 s[0:1], s[38:39]
	ds_add_u32 v8, v224
	s_mov_b64 exec, s[0:1]
	v_cmp_eq_u32_sdwa s[38:39], v196, v4 src0_sel:BYTE_1 src1_sel:DWORD
	v_and_b32_e32 v8, 0xff, v196
	v_lshl_add_u32 v8, v8, 2, v6
	s_and_saveexec_b64 s[0:1], s[38:39]
	ds_add_u32 v8, v224
	s_mov_b64 exec, s[0:1]
	v_cmp_eq_u32_sdwa s[38:39], v196, v4 src0_sel:BYTE_3 src1_sel:DWORD
	v_bfe_u32 v8, v196, 16, 8
	v_lshl_add_u32 v8, v8, 2, v6
	s_and_saveexec_b64 s[0:1], s[38:39]
	ds_add_u32 v8, v224
	s_mov_b64 exec, s[0:1]
	v_cmp_eq_u32_sdwa s[38:39], v197, v4 src0_sel:BYTE_1 src1_sel:DWORD
	v_and_b32_e32 v8, 0xff, v197
	v_lshl_add_u32 v8, v8, 2, v6
	s_and_saveexec_b64 s[0:1], s[38:39]
	ds_add_u32 v8, v224
	s_mov_b64 exec, s[0:1]
	v_cmp_eq_u32_sdwa s[38:39], v197, v4 src0_sel:BYTE_3 src1_sel:DWORD
	v_bfe_u32 v8, v197, 16, 8
	v_lshl_add_u32 v8, v8, 2, v6
	s_and_saveexec_b64 s[0:1], s[38:39]
	ds_add_u32 v8, v224
	s_mov_b64 exec, s[0:1]
	v_cmp_eq_u32_sdwa s[38:39], v198, v4 src0_sel:BYTE_1 src1_sel:DWORD
	v_and_b32_e32 v8, 0xff, v198
	v_lshl_add_u32 v8, v8, 2, v6
	s_and_saveexec_b64 s[0:1], s[38:39]
	ds_add_u32 v8, v224
	s_mov_b64 exec, s[0:1]
	v_cmp_eq_u32_sdwa s[38:39], v198, v4 src0_sel:BYTE_3 src1_sel:DWORD
	v_bfe_u32 v8, v198, 16, 8
	v_lshl_add_u32 v8, v8, 2, v6
	s_and_saveexec_b64 s[0:1], s[38:39]
	ds_add_u32 v8, v224
	s_mov_b64 exec, s[0:1]
	v_cmp_eq_u32_sdwa s[38:39], v199, v4 src0_sel:BYTE_1 src1_sel:DWORD
	v_and_b32_e32 v8, 0xff, v199
	v_lshl_add_u32 v8, v8, 2, v6
	s_and_saveexec_b64 s[0:1], s[38:39]
	ds_add_u32 v8, v224
	s_mov_b64 exec, s[0:1]
	v_cmp_eq_u32_sdwa s[38:39], v199, v4 src0_sel:BYTE_3 src1_sel:DWORD
	v_bfe_u32 v8, v199, 16, 8
	v_lshl_add_u32 v8, v8, 2, v6
	s_and_saveexec_b64 s[0:1], s[38:39]
	ds_add_u32 v8, v224
	s_mov_b64 exec, s[0:1]
	s_cmp_gt_i32 s37, s25
	s_cbranch_scc1 .Lpb_done
	v_cmp_eq_u32_sdwa s[38:39], v192, v4 src0_sel:BYTE_1 src1_sel:DWORD
	v_and_b32_e32 v8, 0xff, v192
	v_lshl_add_u32 v8, v8, 2, v6
	s_and_saveexec_b64 s[0:1], s[38:39]
	ds_add_u32 v8, v224
	s_mov_b64 exec, s[0:1]
	v_cmp_eq_u32_sdwa s[38:39], v192, v4 src0_sel:BYTE_3 src1_sel:DWORD
	v_bfe_u32 v8, v192, 16, 8
	v_lshl_add_u32 v8, v8, 2, v6
	s_and_saveexec_b64 s[0:1], s[38:39]
	ds_add_u32 v8, v224
	s_mov_b64 exec, s[0:1]
	v_cmp_eq_u32_sdwa s[38:39], v193, v4 src0_sel:BYTE_1 src1_sel:DWORD
	v_and_b32_e32 v8, 0xff, v193
	v_lshl_add_u32 v8, v8, 2, v6
	s_and_saveexec_b64 s[0:1], s[38:39]
	ds_add_u32 v8, v224
	s_mov_b64 exec, s[0:1]
	v_cmp_eq_u32_sdwa s[38:39], v193, v4 src0_sel:BYTE_3 src1_sel:DWORD
	v_bfe_u32 v8, v193, 16, 8
	v_lshl_add_u32 v8, v8, 2, v6
	s_and_saveexec_b64 s[0:1], s[38:39]
	ds_add_u32 v8, v224
	s_mov_b64 exec, s[0:1]
	v_cmp_eq_u32_sdwa s[38:39], v194, v4 src0_sel:BYTE_1 src1_sel:DWORD
	v_and_b32_e32 v8, 0xff, v194
	v_lshl_add_u32 v8, v8, 2, v6
	s_and_saveexec_b64 s[0:1], s[38:39]
	ds_add_u32 v8, v224
	s_mov_b64 exec, s[0:1]
	v_cmp_eq_u32_sdwa s[38:39], v194, v4 src0_sel:BYTE_3 src1_sel:DWORD
	v_bfe_u32 v8, v194, 16, 8
	v_lshl_add_u32 v8, v8, 2, v6
	s_and_saveexec_b64 s[0:1], s[38:39]
	ds_add_u32 v8, v224
	s_mov_b64 exec, s[0:1]
	v_cmp_eq_u32_sdwa s[38:39], v195, v4 src0_sel:BYTE_1 src1_sel:DWORD
	v_and_b32_e32 v8, 0xff, v195
	v_lshl_add_u32 v8, v8, 2, v6
	s_and_saveexec_b64 s[0:1], s[38:39]
	ds_add_u32 v8, v224
	s_mov_b64 exec, s[0:1]
	v_cmp_eq_u32_sdwa s[38:39], v195, v4 src0_sel:BYTE_3 src1_sel:DWORD
	v_bfe_u32 v8, v195, 16, 8
	v_lshl_add_u32 v8, v8, 2, v6
	s_and_saveexec_b64 s[0:1], s[38:39]
	ds_add_u32 v8, v224
	s_mov_b64 exec, s[0:1]
	v_cmp_eq_u32_sdwa s[38:39], v184, v4 src0_sel:BYTE_1 src1_sel:DWORD
	v_and_b32_e32 v8, 0xff, v184
	v_lshl_add_u32 v8, v8, 2, v6
	s_and_saveexec_b64 s[0:1], s[38:39]
	ds_add_u32 v8, v224
	s_mov_b64 exec, s[0:1]
	v_cmp_eq_u32_sdwa s[38:39], v184, v4 src0_sel:BYTE_3 src1_sel:DWORD
	v_bfe_u32 v8, v184, 16, 8
	v_lshl_add_u32 v8, v8, 2, v6
	s_and_saveexec_b64 s[0:1], s[38:39]
	ds_add_u32 v8, v224
	s_mov_b64 exec, s[0:1]
	v_cmp_eq_u32_sdwa s[38:39], v185, v4 src0_sel:BYTE_1 src1_sel:DWORD
	v_and_b32_e32 v8, 0xff, v185
	v_lshl_add_u32 v8, v8, 2, v6
	s_and_saveexec_b64 s[0:1], s[38:39]
	ds_add_u32 v8, v224
	s_mov_b64 exec, s[0:1]
	v_cmp_eq_u32_sdwa s[38:39], v185, v4 src0_sel:BYTE_3 src1_sel:DWORD
	v_bfe_u32 v8, v185, 16, 8
	v_lshl_add_u32 v8, v8, 2, v6
	s_and_saveexec_b64 s[0:1], s[38:39]
	ds_add_u32 v8, v224
	s_mov_b64 exec, s[0:1]
	v_cmp_eq_u32_sdwa s[38:39], v186, v4 src0_sel:BYTE_1 src1_sel:DWORD
	v_and_b32_e32 v8, 0xff, v186
	v_lshl_add_u32 v8, v8, 2, v6
	s_and_saveexec_b64 s[0:1], s[38:39]
	ds_add_u32 v8, v224
	s_mov_b64 exec, s[0:1]
	v_cmp_eq_u32_sdwa s[38:39], v186, v4 src0_sel:BYTE_3 src1_sel:DWORD
	v_bfe_u32 v8, v186, 16, 8
	v_lshl_add_u32 v8, v8, 2, v6
	s_and_saveexec_b64 s[0:1], s[38:39]
	ds_add_u32 v8, v224
	s_mov_b64 exec, s[0:1]
	v_cmp_eq_u32_sdwa s[38:39], v187, v4 src0_sel:BYTE_1 src1_sel:DWORD
	v_and_b32_e32 v8, 0xff, v187
	v_lshl_add_u32 v8, v8, 2, v6
	s_and_saveexec_b64 s[0:1], s[38:39]
	ds_add_u32 v8, v224
	s_mov_b64 exec, s[0:1]
	v_cmp_eq_u32_sdwa s[38:39], v187, v4 src0_sel:BYTE_3 src1_sel:DWORD
	v_bfe_u32 v8, v187, 16, 8
	v_lshl_add_u32 v8, v8, 2, v6
	s_and_saveexec_b64 s[0:1], s[38:39]
	ds_add_u32 v8, v224
	s_mov_b64 exec, s[0:1]
	s_cmp_gt_i32 s37, s27
	s_cbranch_scc1 .Lpb_done
	v_cmp_eq_u32_sdwa s[38:39], v168, v4 src0_sel:BYTE_1 src1_sel:DWORD
	v_and_b32_e32 v8, 0xff, v168
	v_lshl_add_u32 v8, v8, 2, v6
	s_and_saveexec_b64 s[0:1], s[38:39]
	ds_add_u32 v8, v224
	s_mov_b64 exec, s[0:1]
	v_cmp_eq_u32_sdwa s[38:39], v168, v4 src0_sel:BYTE_3 src1_sel:DWORD
	v_bfe_u32 v8, v168, 16, 8
	v_lshl_add_u32 v8, v8, 2, v6
	s_and_saveexec_b64 s[0:1], s[38:39]
	ds_add_u32 v8, v224
	s_mov_b64 exec, s[0:1]
	v_cmp_eq_u32_sdwa s[38:39], v169, v4 src0_sel:BYTE_1 src1_sel:DWORD
	v_and_b32_e32 v8, 0xff, v169
	v_lshl_add_u32 v8, v8, 2, v6
	s_and_saveexec_b64 s[0:1], s[38:39]
	ds_add_u32 v8, v224
	s_mov_b64 exec, s[0:1]
	v_cmp_eq_u32_sdwa s[38:39], v169, v4 src0_sel:BYTE_3 src1_sel:DWORD
	v_bfe_u32 v8, v169, 16, 8
	v_lshl_add_u32 v8, v8, 2, v6
	s_and_saveexec_b64 s[0:1], s[38:39]
	ds_add_u32 v8, v224
	s_mov_b64 exec, s[0:1]
	v_cmp_eq_u32_sdwa s[38:39], v170, v4 src0_sel:BYTE_1 src1_sel:DWORD
	v_and_b32_e32 v8, 0xff, v170
	v_lshl_add_u32 v8, v8, 2, v6
	s_and_saveexec_b64 s[0:1], s[38:39]
	ds_add_u32 v8, v224
	s_mov_b64 exec, s[0:1]
	v_cmp_eq_u32_sdwa s[38:39], v170, v4 src0_sel:BYTE_3 src1_sel:DWORD
	v_bfe_u32 v8, v170, 16, 8
	v_lshl_add_u32 v8, v8, 2, v6
	s_and_saveexec_b64 s[0:1], s[38:39]
	ds_add_u32 v8, v224
	s_mov_b64 exec, s[0:1]
	v_cmp_eq_u32_sdwa s[38:39], v171, v4 src0_sel:BYTE_1 src1_sel:DWORD
	v_and_b32_e32 v8, 0xff, v171
	v_lshl_add_u32 v8, v8, 2, v6
	s_and_saveexec_b64 s[0:1], s[38:39]
	ds_add_u32 v8, v224
	s_mov_b64 exec, s[0:1]
	v_cmp_eq_u32_sdwa s[38:39], v171, v4 src0_sel:BYTE_3 src1_sel:DWORD
	v_bfe_u32 v8, v171, 16, 8
	v_lshl_add_u32 v8, v8, 2, v6
	s_and_saveexec_b64 s[0:1], s[38:39]
	ds_add_u32 v8, v224
	s_mov_b64 exec, s[0:1]
	v_cmp_eq_u32_sdwa s[38:39], v148, v4 src0_sel:BYTE_1 src1_sel:DWORD
	v_and_b32_e32 v8, 0xff, v148
	v_lshl_add_u32 v8, v8, 2, v6
	s_and_saveexec_b64 s[0:1], s[38:39]
	ds_add_u32 v8, v224
	s_mov_b64 exec, s[0:1]
	v_cmp_eq_u32_sdwa s[38:39], v148, v4 src0_sel:BYTE_3 src1_sel:DWORD
	v_bfe_u32 v8, v148, 16, 8
	v_lshl_add_u32 v8, v8, 2, v6
	s_and_saveexec_b64 s[0:1], s[38:39]
	ds_add_u32 v8, v224
	s_mov_b64 exec, s[0:1]
	v_cmp_eq_u32_sdwa s[38:39], v149, v4 src0_sel:BYTE_1 src1_sel:DWORD
	v_and_b32_e32 v8, 0xff, v149
	v_lshl_add_u32 v8, v8, 2, v6
	s_and_saveexec_b64 s[0:1], s[38:39]
	ds_add_u32 v8, v224
	s_mov_b64 exec, s[0:1]
	v_cmp_eq_u32_sdwa s[38:39], v149, v4 src0_sel:BYTE_3 src1_sel:DWORD
	v_bfe_u32 v8, v149, 16, 8
	v_lshl_add_u32 v8, v8, 2, v6
	s_and_saveexec_b64 s[0:1], s[38:39]
	ds_add_u32 v8, v224
	s_mov_b64 exec, s[0:1]
	v_cmp_eq_u32_sdwa s[38:39], v150, v4 src0_sel:BYTE_1 src1_sel:DWORD
	v_and_b32_e32 v8, 0xff, v150
	v_lshl_add_u32 v8, v8, 2, v6
	s_and_saveexec_b64 s[0:1], s[38:39]
	ds_add_u32 v8, v224
	s_mov_b64 exec, s[0:1]
	v_cmp_eq_u32_sdwa s[38:39], v150, v4 src0_sel:BYTE_3 src1_sel:DWORD
	v_bfe_u32 v8, v150, 16, 8
	v_lshl_add_u32 v8, v8, 2, v6
	s_and_saveexec_b64 s[0:1], s[38:39]
	ds_add_u32 v8, v224
	s_mov_b64 exec, s[0:1]
	v_cmp_eq_u32_sdwa s[38:39], v151, v4 src0_sel:BYTE_1 src1_sel:DWORD
	v_and_b32_e32 v8, 0xff, v151
	v_lshl_add_u32 v8, v8, 2, v6
	s_and_saveexec_b64 s[0:1], s[38:39]
	ds_add_u32 v8, v224
	s_mov_b64 exec, s[0:1]
	v_cmp_eq_u32_sdwa s[38:39], v151, v4 src0_sel:BYTE_3 src1_sel:DWORD
	v_bfe_u32 v8, v151, 16, 8
	v_lshl_add_u32 v8, v8, 2, v6
	s_and_saveexec_b64 s[0:1], s[38:39]
	ds_add_u32 v8, v224
	s_mov_b64 exec, s[0:1]
.Lpb_done:
	v_add_u32_e32 v7, 0x10000, v7
	s_and_b64 vcc, exec, s[18:19]
	s_cbranch_vccnz .LBB0_581
